# k_final: waves 4-7 enter the main loop half a block late (stagger between SIMD partners)
# baseline (speedup 1.0000x reference)
.LBB1_26:
	s_cmp_lt_u32 s20, 4
	s_cbranch_scc1 .Lfin_nostag
	s_sleep 8
